# speedup vs baseline: 1.0984x; 1.0131x over previous
.Lagg_gloop:
	v_add_u32_e32 v104, 6, v50
	v_cmp_lt_i32_e32 vcc, v104, v51
	s_and_b64 vcc, exec, vcc
	s_cbranch_scc0 .Lagg_glast
	s_waitcnt vmcnt(15)
	v_cvt_pk_f32_fp8_e32 v[96:97], v2
	v_cvt_pk_f32_fp8_sdwa v[98:99], v2 src0_sel:WORD_1
	v_cvt_pk_f32_fp8_e32 v[100:101], v3
	v_cvt_pk_f32_fp8_sdwa v[102:103], v3 src0_sel:WORD_1
	v_pk_add_f32 v[88:89], v[88:89], v[96:97]
	v_pk_add_f32 v[90:91], v[90:91], v[98:99]
	v_pk_add_f32 v[92:93], v[92:93], v[100:101]
	v_pk_add_f32 v[94:95], v[94:95], v[102:103]
	v_cvt_pk_f32_fp8_e32 v[96:97], v4
	v_cvt_pk_f32_fp8_sdwa v[98:99], v4 src0_sel:WORD_1
	v_cvt_pk_f32_fp8_e32 v[100:101], v5
	v_cvt_pk_f32_fp8_sdwa v[102:103], v5 src0_sel:WORD_1
	v_pk_add_f32 v[76:77], v[76:77], v[96:97]
	v_pk_add_f32 v[80:81], v[80:81], v[98:99]
	v_pk_add_f32 v[84:85], v[84:85], v[100:101]
	v_pk_add_f32 v[86:87], v[86:87], v[102:103]
	v_cvt_pk_f32_fp8_e32 v[96:97], v6
	v_cvt_pk_f32_fp8_sdwa v[98:99], v6 src0_sel:WORD_1
	v_cvt_pk_f32_fp8_e32 v[100:101], v7
	v_cvt_pk_f32_fp8_sdwa v[102:103], v7 src0_sel:WORD_1
	v_pk_add_f32 v[72:73], v[72:73], v[96:97]
	v_pk_add_f32 v[74:75], v[74:75], v[98:99]
	v_pk_add_f32 v[78:79], v[78:79], v[100:101]
	v_pk_add_f32 v[82:83], v[82:83], v[102:103]
	v_cvt_pk_f32_fp8_e32 v[96:97], v8
	v_cvt_pk_f32_fp8_sdwa v[98:99], v8 src0_sel:WORD_1
	v_cvt_pk_f32_fp8_e32 v[100:101], v9
	v_cvt_pk_f32_fp8_sdwa v[102:103], v9 src0_sel:WORD_1
	v_pk_add_f32 v[64:65], v[64:65], v[96:97]
	v_pk_add_f32 v[66:67], v[66:67], v[98:99]
	v_pk_add_f32 v[68:69], v[68:69], v[100:101]
	v_pk_add_f32 v[70:71], v[70:71], v[102:103]
	v_add_u32_e32 v104, 6, v50
	v_cmp_lt_i32_e32 vcc, v104, v51
	v_lshlrev_b32_e32 v105, 7, v56
	v_add_u32_e32 v106, 6, v104
	v_min_i32_e32 v106, v106, v55
	v_cndmask_b32_e32 v105, v62, v105, vcc
	v_or_b32_e32 v105, v54, v105
	global_load_dwordx4 v[2:5], v105, s[4:5]
	global_load_dwordx4 v[6:9], v105, s[4:5] offset:64
	v_lshlrev_b32_e32 v106, 2, v106
	global_load_dword v56, v106, s[8:9]
	s_waitcnt vmcnt(15)
	v_cvt_pk_f32_fp8_e32 v[96:97], v10
	v_cvt_pk_f32_fp8_sdwa v[98:99], v10 src0_sel:WORD_1
	v_cvt_pk_f32_fp8_e32 v[100:101], v11
	v_cvt_pk_f32_fp8_sdwa v[102:103], v11 src0_sel:WORD_1
	v_pk_add_f32 v[88:89], v[88:89], v[96:97]
	v_pk_add_f32 v[90:91], v[90:91], v[98:99]
	v_pk_add_f32 v[92:93], v[92:93], v[100:101]
	v_pk_add_f32 v[94:95], v[94:95], v[102:103]
	v_cvt_pk_f32_fp8_e32 v[96:97], v12
	v_cvt_pk_f32_fp8_sdwa v[98:99], v12 src0_sel:WORD_1
	v_cvt_pk_f32_fp8_e32 v[100:101], v13
	v_cvt_pk_f32_fp8_sdwa v[102:103], v13 src0_sel:WORD_1
	v_pk_add_f32 v[76:77], v[76:77], v[96:97]
	v_pk_add_f32 v[80:81], v[80:81], v[98:99]
	v_pk_add_f32 v[84:85], v[84:85], v[100:101]
	v_pk_add_f32 v[86:87], v[86:87], v[102:103]
	v_cvt_pk_f32_fp8_e32 v[96:97], v14
	v_cvt_pk_f32_fp8_sdwa v[98:99], v14 src0_sel:WORD_1
	v_cvt_pk_f32_fp8_e32 v[100:101], v15
	v_cvt_pk_f32_fp8_sdwa v[102:103], v15 src0_sel:WORD_1
	v_pk_add_f32 v[72:73], v[72:73], v[96:97]
	v_pk_add_f32 v[74:75], v[74:75], v[98:99]
	v_pk_add_f32 v[78:79], v[78:79], v[100:101]
	v_pk_add_f32 v[82:83], v[82:83], v[102:103]
	v_cvt_pk_f32_fp8_e32 v[96:97], v16
	v_cvt_pk_f32_fp8_sdwa v[98:99], v16 src0_sel:WORD_1
	v_cvt_pk_f32_fp8_e32 v[100:101], v17
	v_cvt_pk_f32_fp8_sdwa v[102:103], v17 src0_sel:WORD_1
	v_pk_add_f32 v[64:65], v[64:65], v[96:97]
	v_pk_add_f32 v[66:67], v[66:67], v[98:99]
	v_pk_add_f32 v[68:69], v[68:69], v[100:101]
	v_pk_add_f32 v[70:71], v[70:71], v[102:103]
	v_add_u32_e32 v104, 7, v50
	v_cmp_lt_i32_e32 vcc, v104, v51
	v_lshlrev_b32_e32 v105, 7, v57
	v_add_u32_e32 v106, 6, v104
	v_min_i32_e32 v106, v106, v55
	v_cndmask_b32_e32 v105, v62, v105, vcc
	v_or_b32_e32 v105, v54, v105
	global_load_dwordx4 v[10:13], v105, s[4:5]
	global_load_dwordx4 v[14:17], v105, s[4:5] offset:64
	v_lshlrev_b32_e32 v106, 2, v106
	global_load_dword v57, v106, s[8:9]
	s_waitcnt vmcnt(15)
	v_cvt_pk_f32_fp8_e32 v[96:97], v18
	v_cvt_pk_f32_fp8_sdwa v[98:99], v18 src0_sel:WORD_1
	v_cvt_pk_f32_fp8_e32 v[100:101], v19
	v_cvt_pk_f32_fp8_sdwa v[102:103], v19 src0_sel:WORD_1
	v_pk_add_f32 v[88:89], v[88:89], v[96:97]
	v_pk_add_f32 v[90:91], v[90:91], v[98:99]
	v_pk_add_f32 v[92:93], v[92:93], v[100:101]
	v_pk_add_f32 v[94:95], v[94:95], v[102:103]
	v_cvt_pk_f32_fp8_e32 v[96:97], v20
	v_cvt_pk_f32_fp8_sdwa v[98:99], v20 src0_sel:WORD_1
	v_cvt_pk_f32_fp8_e32 v[100:101], v21
	v_cvt_pk_f32_fp8_sdwa v[102:103], v21 src0_sel:WORD_1
	v_pk_add_f32 v[76:77], v[76:77], v[96:97]
	v_pk_add_f32 v[80:81], v[80:81], v[98:99]
	v_pk_add_f32 v[84:85], v[84:85], v[100:101]
	v_pk_add_f32 v[86:87], v[86:87], v[102:103]
	v_cvt_pk_f32_fp8_e32 v[96:97], v22
	v_cvt_pk_f32_fp8_sdwa v[98:99], v22 src0_sel:WORD_1
	v_cvt_pk_f32_fp8_e32 v[100:101], v23
	v_cvt_pk_f32_fp8_sdwa v[102:103], v23 src0_sel:WORD_1
	v_pk_add_f32 v[72:73], v[72:73], v[96:97]
	v_pk_add_f32 v[74:75], v[74:75], v[98:99]
	v_pk_add_f32 v[78:79], v[78:79], v[100:101]
	v_pk_add_f32 v[82:83], v[82:83], v[102:103]
	v_cvt_pk_f32_fp8_e32 v[96:97], v24
	v_cvt_pk_f32_fp8_sdwa v[98:99], v24 src0_sel:WORD_1
	v_cvt_pk_f32_fp8_e32 v[100:101], v25
	v_cvt_pk_f32_fp8_sdwa v[102:103], v25 src0_sel:WORD_1
	v_pk_add_f32 v[64:65], v[64:65], v[96:97]
	v_pk_add_f32 v[66:67], v[66:67], v[98:99]
	v_pk_add_f32 v[68:69], v[68:69], v[100:101]
	v_pk_add_f32 v[70:71], v[70:71], v[102:103]
	v_add_u32_e32 v104, 8, v50
	v_cmp_lt_i32_e32 vcc, v104, v51
	v_lshlrev_b32_e32 v105, 7, v58
	v_add_u32_e32 v106, 6, v104
	v_min_i32_e32 v106, v106, v55
	v_cndmask_b32_e32 v105, v62, v105, vcc
	v_or_b32_e32 v105, v54, v105
	global_load_dwordx4 v[18:21], v105, s[4:5]
	global_load_dwordx4 v[22:25], v105, s[4:5] offset:64
	v_lshlrev_b32_e32 v106, 2, v106
	global_load_dword v58, v106, s[8:9]
	s_waitcnt vmcnt(15)
	v_cvt_pk_f32_fp8_e32 v[96:97], v26
	v_cvt_pk_f32_fp8_sdwa v[98:99], v26 src0_sel:WORD_1
	v_cvt_pk_f32_fp8_e32 v[100:101], v27
	v_cvt_pk_f32_fp8_sdwa v[102:103], v27 src0_sel:WORD_1
	v_pk_add_f32 v[88:89], v[88:89], v[96:97]
	v_pk_add_f32 v[90:91], v[90:91], v[98:99]
	v_pk_add_f32 v[92:93], v[92:93], v[100:101]
	v_pk_add_f32 v[94:95], v[94:95], v[102:103]
	v_cvt_pk_f32_fp8_e32 v[96:97], v28
	v_cvt_pk_f32_fp8_sdwa v[98:99], v28 src0_sel:WORD_1
	v_cvt_pk_f32_fp8_e32 v[100:101], v29
	v_cvt_pk_f32_fp8_sdwa v[102:103], v29 src0_sel:WORD_1
	v_pk_add_f32 v[76:77], v[76:77], v[96:97]
	v_pk_add_f32 v[80:81], v[80:81], v[98:99]
	v_pk_add_f32 v[84:85], v[84:85], v[100:101]
	v_pk_add_f32 v[86:87], v[86:87], v[102:103]
	v_cvt_pk_f32_fp8_e32 v[96:97], v30
	v_cvt_pk_f32_fp8_sdwa v[98:99], v30 src0_sel:WORD_1
	v_cvt_pk_f32_fp8_e32 v[100:101], v31
	v_cvt_pk_f32_fp8_sdwa v[102:103], v31 src0_sel:WORD_1
	v_pk_add_f32 v[72:73], v[72:73], v[96:97]
	v_pk_add_f32 v[74:75], v[74:75], v[98:99]
	v_pk_add_f32 v[78:79], v[78:79], v[100:101]
	v_pk_add_f32 v[82:83], v[82:83], v[102:103]
	v_cvt_pk_f32_fp8_e32 v[96:97], v32
	v_cvt_pk_f32_fp8_sdwa v[98:99], v32 src0_sel:WORD_1
	v_cvt_pk_f32_fp8_e32 v[100:101], v33
	v_cvt_pk_f32_fp8_sdwa v[102:103], v33 src0_sel:WORD_1
	v_pk_add_f32 v[64:65], v[64:65], v[96:97]
	v_pk_add_f32 v[66:67], v[66:67], v[98:99]
	v_pk_add_f32 v[68:69], v[68:69], v[100:101]
	v_pk_add_f32 v[70:71], v[70:71], v[102:103]
	v_add_u32_e32 v104, 9, v50
	v_cmp_lt_i32_e32 vcc, v104, v51
	v_lshlrev_b32_e32 v105, 7, v59
	v_add_u32_e32 v106, 6, v104
	v_min_i32_e32 v106, v106, v55
	v_cndmask_b32_e32 v105, v62, v105, vcc
	v_or_b32_e32 v105, v54, v105
	global_load_dwordx4 v[26:29], v105, s[4:5]
	global_load_dwordx4 v[30:33], v105, s[4:5] offset:64
	v_lshlrev_b32_e32 v106, 2, v106
	global_load_dword v59, v106, s[8:9]
	s_waitcnt vmcnt(15)
	v_cvt_pk_f32_fp8_e32 v[96:97], v34
	v_cvt_pk_f32_fp8_sdwa v[98:99], v34 src0_sel:WORD_1
	v_cvt_pk_f32_fp8_e32 v[100:101], v35
	v_cvt_pk_f32_fp8_sdwa v[102:103], v35 src0_sel:WORD_1
	v_pk_add_f32 v[88:89], v[88:89], v[96:97]
	v_pk_add_f32 v[90:91], v[90:91], v[98:99]
	v_pk_add_f32 v[92:93], v[92:93], v[100:101]
	v_pk_add_f32 v[94:95], v[94:95], v[102:103]
	v_cvt_pk_f32_fp8_e32 v[96:97], v36
	v_cvt_pk_f32_fp8_sdwa v[98:99], v36 src0_sel:WORD_1
	v_cvt_pk_f32_fp8_e32 v[100:101], v37
	v_cvt_pk_f32_fp8_sdwa v[102:103], v37 src0_sel:WORD_1
	v_pk_add_f32 v[76:77], v[76:77], v[96:97]
	v_pk_add_f32 v[80:81], v[80:81], v[98:99]
	v_pk_add_f32 v[84:85], v[84:85], v[100:101]
	v_pk_add_f32 v[86:87], v[86:87], v[102:103]
	v_cvt_pk_f32_fp8_e32 v[96:97], v38
	v_cvt_pk_f32_fp8_sdwa v[98:99], v38 src0_sel:WORD_1
	v_cvt_pk_f32_fp8_e32 v[100:101], v39
	v_cvt_pk_f32_fp8_sdwa v[102:103], v39 src0_sel:WORD_1
	v_pk_add_f32 v[72:73], v[72:73], v[96:97]
	v_pk_add_f32 v[74:75], v[74:75], v[98:99]
	v_pk_add_f32 v[78:79], v[78:79], v[100:101]
	v_pk_add_f32 v[82:83], v[82:83], v[102:103]
	v_cvt_pk_f32_fp8_e32 v[96:97], v40
	v_cvt_pk_f32_fp8_sdwa v[98:99], v40 src0_sel:WORD_1
	v_cvt_pk_f32_fp8_e32 v[100:101], v41
	v_cvt_pk_f32_fp8_sdwa v[102:103], v41 src0_sel:WORD_1
	v_pk_add_f32 v[64:65], v[64:65], v[96:97]
	v_pk_add_f32 v[66:67], v[66:67], v[98:99]
	v_pk_add_f32 v[68:69], v[68:69], v[100:101]
	v_pk_add_f32 v[70:71], v[70:71], v[102:103]
	v_add_u32_e32 v104, 10, v50
	v_cmp_lt_i32_e32 vcc, v104, v51
	v_lshlrev_b32_e32 v105, 7, v60
	v_add_u32_e32 v106, 6, v104
	v_min_i32_e32 v106, v106, v55
	v_cndmask_b32_e32 v105, v62, v105, vcc
	v_or_b32_e32 v105, v54, v105
	global_load_dwordx4 v[34:37], v105, s[4:5]
	global_load_dwordx4 v[38:41], v105, s[4:5] offset:64
	v_lshlrev_b32_e32 v106, 2, v106
	global_load_dword v60, v106, s[8:9]
	s_waitcnt vmcnt(15)
	v_cvt_pk_f32_fp8_e32 v[96:97], v42
	v_cvt_pk_f32_fp8_sdwa v[98:99], v42 src0_sel:WORD_1
	v_cvt_pk_f32_fp8_e32 v[100:101], v43
	v_cvt_pk_f32_fp8_sdwa v[102:103], v43 src0_sel:WORD_1
	v_pk_add_f32 v[88:89], v[88:89], v[96:97]
	v_pk_add_f32 v[90:91], v[90:91], v[98:99]
	v_pk_add_f32 v[92:93], v[92:93], v[100:101]
	v_pk_add_f32 v[94:95], v[94:95], v[102:103]
	v_cvt_pk_f32_fp8_e32 v[96:97], v44
	v_cvt_pk_f32_fp8_sdwa v[98:99], v44 src0_sel:WORD_1
	v_cvt_pk_f32_fp8_e32 v[100:101], v45
	v_cvt_pk_f32_fp8_sdwa v[102:103], v45 src0_sel:WORD_1
	v_pk_add_f32 v[76:77], v[76:77], v[96:97]
	v_pk_add_f32 v[80:81], v[80:81], v[98:99]
	v_pk_add_f32 v[84:85], v[84:85], v[100:101]
	v_pk_add_f32 v[86:87], v[86:87], v[102:103]
	v_cvt_pk_f32_fp8_e32 v[96:97], v46
	v_cvt_pk_f32_fp8_sdwa v[98:99], v46 src0_sel:WORD_1
	v_cvt_pk_f32_fp8_e32 v[100:101], v47
	v_cvt_pk_f32_fp8_sdwa v[102:103], v47 src0_sel:WORD_1
	v_pk_add_f32 v[72:73], v[72:73], v[96:97]
	v_pk_add_f32 v[74:75], v[74:75], v[98:99]
	v_pk_add_f32 v[78:79], v[78:79], v[100:101]
	v_pk_add_f32 v[82:83], v[82:83], v[102:103]
	v_cvt_pk_f32_fp8_e32 v[96:97], v48
	v_cvt_pk_f32_fp8_sdwa v[98:99], v48 src0_sel:WORD_1
	v_cvt_pk_f32_fp8_e32 v[100:101], v49
	v_cvt_pk_f32_fp8_sdwa v[102:103], v49 src0_sel:WORD_1
	v_pk_add_f32 v[64:65], v[64:65], v[96:97]
	v_pk_add_f32 v[66:67], v[66:67], v[98:99]
	v_pk_add_f32 v[68:69], v[68:69], v[100:101]
	v_pk_add_f32 v[70:71], v[70:71], v[102:103]
	v_add_u32_e32 v104, 11, v50
	v_cmp_lt_i32_e32 vcc, v104, v51
	v_lshlrev_b32_e32 v105, 7, v61
	v_add_u32_e32 v106, 6, v104
	v_min_i32_e32 v106, v106, v55
	v_cndmask_b32_e32 v105, v62, v105, vcc
	v_or_b32_e32 v105, v54, v105
	global_load_dwordx4 v[42:45], v105, s[4:5]
	global_load_dwordx4 v[46:49], v105, s[4:5] offset:64
	v_lshlrev_b32_e32 v106, 2, v106
	global_load_dword v61, v106, s[8:9]
	v_add_u32_e32 v50, 6, v50
	s_branch .Lagg_gloop
.Lagg_glast:
	s_waitcnt vmcnt(16)
	v_cvt_pk_f32_fp8_e32 v[96:97], v2
	v_cvt_pk_f32_fp8_sdwa v[98:99], v2 src0_sel:WORD_1
	v_cvt_pk_f32_fp8_e32 v[100:101], v3
	v_cvt_pk_f32_fp8_sdwa v[102:103], v3 src0_sel:WORD_1
	v_pk_add_f32 v[88:89], v[88:89], v[96:97]
	v_pk_add_f32 v[90:91], v[90:91], v[98:99]
	v_pk_add_f32 v[92:93], v[92:93], v[100:101]
	v_pk_add_f32 v[94:95], v[94:95], v[102:103]
	v_cvt_pk_f32_fp8_e32 v[96:97], v4
	v_cvt_pk_f32_fp8_sdwa v[98:99], v4 src0_sel:WORD_1
	v_cvt_pk_f32_fp8_e32 v[100:101], v5
	v_cvt_pk_f32_fp8_sdwa v[102:103], v5 src0_sel:WORD_1
	v_pk_add_f32 v[76:77], v[76:77], v[96:97]
	v_pk_add_f32 v[80:81], v[80:81], v[98:99]
	v_pk_add_f32 v[84:85], v[84:85], v[100:101]
	v_pk_add_f32 v[86:87], v[86:87], v[102:103]
	v_cvt_pk_f32_fp8_e32 v[96:97], v6
	v_cvt_pk_f32_fp8_sdwa v[98:99], v6 src0_sel:WORD_1
	v_cvt_pk_f32_fp8_e32 v[100:101], v7
	v_cvt_pk_f32_fp8_sdwa v[102:103], v7 src0_sel:WORD_1
	v_pk_add_f32 v[72:73], v[72:73], v[96:97]
	v_pk_add_f32 v[74:75], v[74:75], v[98:99]
	v_pk_add_f32 v[78:79], v[78:79], v[100:101]
	v_pk_add_f32 v[82:83], v[82:83], v[102:103]
	v_cvt_pk_f32_fp8_e32 v[96:97], v8
	v_cvt_pk_f32_fp8_sdwa v[98:99], v8 src0_sel:WORD_1
	v_cvt_pk_f32_fp8_e32 v[100:101], v9
	v_cvt_pk_f32_fp8_sdwa v[102:103], v9 src0_sel:WORD_1
	v_pk_add_f32 v[64:65], v[64:65], v[96:97]
	v_pk_add_f32 v[66:67], v[66:67], v[98:99]
	v_pk_add_f32 v[68:69], v[68:69], v[100:101]
	v_pk_add_f32 v[70:71], v[70:71], v[102:103]
	s_waitcnt vmcnt(13)
	v_cvt_pk_f32_fp8_e32 v[96:97], v10
	v_cvt_pk_f32_fp8_sdwa v[98:99], v10 src0_sel:WORD_1
	v_cvt_pk_f32_fp8_e32 v[100:101], v11
	v_cvt_pk_f32_fp8_sdwa v[102:103], v11 src0_sel:WORD_1
	v_pk_add_f32 v[88:89], v[88:89], v[96:97]
	v_pk_add_f32 v[90:91], v[90:91], v[98:99]
	v_pk_add_f32 v[92:93], v[92:93], v[100:101]
	v_pk_add_f32 v[94:95], v[94:95], v[102:103]
	v_cvt_pk_f32_fp8_e32 v[96:97], v12
	v_cvt_pk_f32_fp8_sdwa v[98:99], v12 src0_sel:WORD_1
	v_cvt_pk_f32_fp8_e32 v[100:101], v13
	v_cvt_pk_f32_fp8_sdwa v[102:103], v13 src0_sel:WORD_1
	v_pk_add_f32 v[76:77], v[76:77], v[96:97]
	v_pk_add_f32 v[80:81], v[80:81], v[98:99]
	v_pk_add_f32 v[84:85], v[84:85], v[100:101]
	v_pk_add_f32 v[86:87], v[86:87], v[102:103]
	v_cvt_pk_f32_fp8_e32 v[96:97], v14
	v_cvt_pk_f32_fp8_sdwa v[98:99], v14 src0_sel:WORD_1
	v_cvt_pk_f32_fp8_e32 v[100:101], v15
	v_cvt_pk_f32_fp8_sdwa v[102:103], v15 src0_sel:WORD_1
	v_pk_add_f32 v[72:73], v[72:73], v[96:97]
	v_pk_add_f32 v[74:75], v[74:75], v[98:99]
	v_pk_add_f32 v[78:79], v[78:79], v[100:101]
	v_pk_add_f32 v[82:83], v[82:83], v[102:103]
	v_cvt_pk_f32_fp8_e32 v[96:97], v16
	v_cvt_pk_f32_fp8_sdwa v[98:99], v16 src0_sel:WORD_1
	v_cvt_pk_f32_fp8_e32 v[100:101], v17
	v_cvt_pk_f32_fp8_sdwa v[102:103], v17 src0_sel:WORD_1
	v_pk_add_f32 v[64:65], v[64:65], v[96:97]
	v_pk_add_f32 v[66:67], v[66:67], v[98:99]
	v_pk_add_f32 v[68:69], v[68:69], v[100:101]
	v_pk_add_f32 v[70:71], v[70:71], v[102:103]
	s_waitcnt vmcnt(10)
	v_cvt_pk_f32_fp8_e32 v[96:97], v18
	v_cvt_pk_f32_fp8_sdwa v[98:99], v18 src0_sel:WORD_1
	v_cvt_pk_f32_fp8_e32 v[100:101], v19
	v_cvt_pk_f32_fp8_sdwa v[102:103], v19 src0_sel:WORD_1
	v_pk_add_f32 v[88:89], v[88:89], v[96:97]
	v_pk_add_f32 v[90:91], v[90:91], v[98:99]
	v_pk_add_f32 v[92:93], v[92:93], v[100:101]
	v_pk_add_f32 v[94:95], v[94:95], v[102:103]
	v_cvt_pk_f32_fp8_e32 v[96:97], v20
	v_cvt_pk_f32_fp8_sdwa v[98:99], v20 src0_sel:WORD_1
	v_cvt_pk_f32_fp8_e32 v[100:101], v21
	v_cvt_pk_f32_fp8_sdwa v[102:103], v21 src0_sel:WORD_1
	v_pk_add_f32 v[76:77], v[76:77], v[96:97]
	v_pk_add_f32 v[80:81], v[80:81], v[98:99]
	v_pk_add_f32 v[84:85], v[84:85], v[100:101]
	v_pk_add_f32 v[86:87], v[86:87], v[102:103]
	v_cvt_pk_f32_fp8_e32 v[96:97], v22
	v_cvt_pk_f32_fp8_sdwa v[98:99], v22 src0_sel:WORD_1
	v_cvt_pk_f32_fp8_e32 v[100:101], v23
	v_cvt_pk_f32_fp8_sdwa v[102:103], v23 src0_sel:WORD_1
	v_pk_add_f32 v[72:73], v[72:73], v[96:97]
	v_pk_add_f32 v[74:75], v[74:75], v[98:99]
	v_pk_add_f32 v[78:79], v[78:79], v[100:101]
	v_pk_add_f32 v[82:83], v[82:83], v[102:103]
	v_cvt_pk_f32_fp8_e32 v[96:97], v24
	v_cvt_pk_f32_fp8_sdwa v[98:99], v24 src0_sel:WORD_1
	v_cvt_pk_f32_fp8_e32 v[100:101], v25
	v_cvt_pk_f32_fp8_sdwa v[102:103], v25 src0_sel:WORD_1
	v_pk_add_f32 v[64:65], v[64:65], v[96:97]
	v_pk_add_f32 v[66:67], v[66:67], v[98:99]
	v_pk_add_f32 v[68:69], v[68:69], v[100:101]
	v_pk_add_f32 v[70:71], v[70:71], v[102:103]
	s_waitcnt vmcnt(7)
	v_cvt_pk_f32_fp8_e32 v[96:97], v26
	v_cvt_pk_f32_fp8_sdwa v[98:99], v26 src0_sel:WORD_1
	v_cvt_pk_f32_fp8_e32 v[100:101], v27
	v_cvt_pk_f32_fp8_sdwa v[102:103], v27 src0_sel:WORD_1
	v_pk_add_f32 v[88:89], v[88:89], v[96:97]
	v_pk_add_f32 v[90:91], v[90:91], v[98:99]
	v_pk_add_f32 v[92:93], v[92:93], v[100:101]
	v_pk_add_f32 v[94:95], v[94:95], v[102:103]
	v_cvt_pk_f32_fp8_e32 v[96:97], v28
	v_cvt_pk_f32_fp8_sdwa v[98:99], v28 src0_sel:WORD_1
	v_cvt_pk_f32_fp8_e32 v[100:101], v29
	v_cvt_pk_f32_fp8_sdwa v[102:103], v29 src0_sel:WORD_1
	v_pk_add_f32 v[76:77], v[76:77], v[96:97]
	v_pk_add_f32 v[80:81], v[80:81], v[98:99]
	v_pk_add_f32 v[84:85], v[84:85], v[100:101]
	v_pk_add_f32 v[86:87], v[86:87], v[102:103]
	v_cvt_pk_f32_fp8_e32 v[96:97], v30
	v_cvt_pk_f32_fp8_sdwa v[98:99], v30 src0_sel:WORD_1
	v_cvt_pk_f32_fp8_e32 v[100:101], v31
	v_cvt_pk_f32_fp8_sdwa v[102:103], v31 src0_sel:WORD_1
	v_pk_add_f32 v[72:73], v[72:73], v[96:97]
	v_pk_add_f32 v[74:75], v[74:75], v[98:99]
	v_pk_add_f32 v[78:79], v[78:79], v[100:101]
	v_pk_add_f32 v[82:83], v[82:83], v[102:103]
	v_cvt_pk_f32_fp8_e32 v[96:97], v32
	v_cvt_pk_f32_fp8_sdwa v[98:99], v32 src0_sel:WORD_1
	v_cvt_pk_f32_fp8_e32 v[100:101], v33
	v_cvt_pk_f32_fp8_sdwa v[102:103], v33 src0_sel:WORD_1
	v_pk_add_f32 v[64:65], v[64:65], v[96:97]
	v_pk_add_f32 v[66:67], v[66:67], v[98:99]
	v_pk_add_f32 v[68:69], v[68:69], v[100:101]
	v_pk_add_f32 v[70:71], v[70:71], v[102:103]
	s_waitcnt vmcnt(4)
	v_cvt_pk_f32_fp8_e32 v[96:97], v34
	v_cvt_pk_f32_fp8_sdwa v[98:99], v34 src0_sel:WORD_1
	v_cvt_pk_f32_fp8_e32 v[100:101], v35
	v_cvt_pk_f32_fp8_sdwa v[102:103], v35 src0_sel:WORD_1
	v_pk_add_f32 v[88:89], v[88:89], v[96:97]
	v_pk_add_f32 v[90:91], v[90:91], v[98:99]
	v_pk_add_f32 v[92:93], v[92:93], v[100:101]
	v_pk_add_f32 v[94:95], v[94:95], v[102:103]
	v_cvt_pk_f32_fp8_e32 v[96:97], v36
	v_cvt_pk_f32_fp8_sdwa v[98:99], v36 src0_sel:WORD_1
	v_cvt_pk_f32_fp8_e32 v[100:101], v37
	v_cvt_pk_f32_fp8_sdwa v[102:103], v37 src0_sel:WORD_1
	v_pk_add_f32 v[76:77], v[76:77], v[96:97]
	v_pk_add_f32 v[80:81], v[80:81], v[98:99]
	v_pk_add_f32 v[84:85], v[84:85], v[100:101]
	v_pk_add_f32 v[86:87], v[86:87], v[102:103]
	v_cvt_pk_f32_fp8_e32 v[96:97], v38
	v_cvt_pk_f32_fp8_sdwa v[98:99], v38 src0_sel:WORD_1
	v_cvt_pk_f32_fp8_e32 v[100:101], v39
	v_cvt_pk_f32_fp8_sdwa v[102:103], v39 src0_sel:WORD_1
	v_pk_add_f32 v[72:73], v[72:73], v[96:97]
	v_pk_add_f32 v[74:75], v[74:75], v[98:99]
	v_pk_add_f32 v[78:79], v[78:79], v[100:101]
	v_pk_add_f32 v[82:83], v[82:83], v[102:103]
	v_cvt_pk_f32_fp8_e32 v[96:97], v40
	v_cvt_pk_f32_fp8_sdwa v[98:99], v40 src0_sel:WORD_1
	v_cvt_pk_f32_fp8_e32 v[100:101], v41
	v_cvt_pk_f32_fp8_sdwa v[102:103], v41 src0_sel:WORD_1
	v_pk_add_f32 v[64:65], v[64:65], v[96:97]
	v_pk_add_f32 v[66:67], v[66:67], v[98:99]
	v_pk_add_f32 v[68:69], v[68:69], v[100:101]
	v_pk_add_f32 v[70:71], v[70:71], v[102:103]
	s_waitcnt vmcnt(1)
	v_cvt_pk_f32_fp8_e32 v[96:97], v42
	v_cvt_pk_f32_fp8_sdwa v[98:99], v42 src0_sel:WORD_1
	v_cvt_pk_f32_fp8_e32 v[100:101], v43
	v_cvt_pk_f32_fp8_sdwa v[102:103], v43 src0_sel:WORD_1
	v_pk_add_f32 v[88:89], v[88:89], v[96:97]
	v_pk_add_f32 v[90:91], v[90:91], v[98:99]
	v_pk_add_f32 v[92:93], v[92:93], v[100:101]
	v_pk_add_f32 v[94:95], v[94:95], v[102:103]
	v_cvt_pk_f32_fp8_e32 v[96:97], v44
	v_cvt_pk_f32_fp8_sdwa v[98:99], v44 src0_sel:WORD_1
	v_cvt_pk_f32_fp8_e32 v[100:101], v45
	v_cvt_pk_f32_fp8_sdwa v[102:103], v45 src0_sel:WORD_1
	v_pk_add_f32 v[76:77], v[76:77], v[96:97]
	v_pk_add_f32 v[80:81], v[80:81], v[98:99]
	v_pk_add_f32 v[84:85], v[84:85], v[100:101]
	v_pk_add_f32 v[86:87], v[86:87], v[102:103]
	v_cvt_pk_f32_fp8_e32 v[96:97], v46
	v_cvt_pk_f32_fp8_sdwa v[98:99], v46 src0_sel:WORD_1
	v_cvt_pk_f32_fp8_e32 v[100:101], v47
	v_cvt_pk_f32_fp8_sdwa v[102:103], v47 src0_sel:WORD_1
	v_pk_add_f32 v[72:73], v[72:73], v[96:97]
	v_pk_add_f32 v[74:75], v[74:75], v[98:99]
	v_pk_add_f32 v[78:79], v[78:79], v[100:101]
	v_pk_add_f32 v[82:83], v[82:83], v[102:103]
	v_cvt_pk_f32_fp8_e32 v[96:97], v48
	v_cvt_pk_f32_fp8_sdwa v[98:99], v48 src0_sel:WORD_1
	v_cvt_pk_f32_fp8_e32 v[100:101], v49
	v_cvt_pk_f32_fp8_sdwa v[102:103], v49 src0_sel:WORD_1
	v_pk_add_f32 v[64:65], v[64:65], v[96:97]
	v_pk_add_f32 v[66:67], v[66:67], v[98:99]
	v_pk_add_f32 v[68:69], v[68:69], v[100:101]
	v_pk_add_f32 v[70:71], v[70:71], v[102:103]
	s_waitcnt vmcnt(0)
